# out-projection epilogue: residual loads issued 8 pieces ahead, stores not waited for
# baseline (speedup 1.0000x reference)
.LBB0_760:
	v_mov_b32_e32 v2, v190
	v_mov_b32_e32 v8, v1
	s_lshl_b32 s41, s71, 8
	s_nop 15
	s_nop 15
	s_or_b32 s41, s41, s64
	v_lshl_add_u32 v2, v2, 3, s41
	s_ashr_i32 s41, s44, 31
	s_lshr_b32 s41, s41, 28
	s_add_i32 s41, s44, s41
	s_lshl_b32 s39, s44, 8
	s_ashr_i32 s41, s41, 4
	s_add_i32 s39, s39, s63
	s_mul_hi_i32 s44, s41, 0xc000
	s_mul_i32 s41, s41, 0xc000
	s_add_u32 s46, s6, s41
	v_ashrrev_i32_e32 v3, 31, v2
	s_addc_u32 s47, s7, s44
	v_lshlrev_b64 v[2:3], 2, v[2:3]
	v_add_u32_e32 v8, s39, v8
	v_lshl_add_u64 v[10:11], s[46:47], 0, v[2:3]
	v_ashrrev_i32_e32 v9, 31, v8
	v_add_co_u32_e32 v4, vcc, s70, v10
	v_lshlrev_b64 v[8:9], 13, v[8:9]
	s_nop 0
	v_addc_co_u32_e32 v5, vcc, 0, v11, vcc
	v_lshl_add_u64 v[12:13], s[10:11], 0, v[8:9]
	global_load_dwordx4 v[4:7], v[4:5], off
	v_lshl_add_u64 v[18:19], v[12:13], 0, v[2:3]
	v_lshl_add_u64 v[12:13], s[8:9], 0, v[8:9]
	v_lshl_add_u64 v[10:11], v[10:11], 0, s[20:21]
	v_lshl_add_u64 v[32:33], v[12:13], 0, v[2:3]
	global_load_dwordx4 v[20:23], v[10:11], off offset:528
	global_load_dwordx4 v[24:27], v[10:11], off offset:16
	global_load_dwordx4 v[28:31], v[10:11], off offset:512
	s_and_b64 vcc, exec, s[0:1]
	s_mov_b64 s[0:1], -1
	s_sub_u32 s48, s8, s10
	s_subb_u32 s49, s9, s11
	v_lshl_add_u64 v[236:237], s[10:11], 0, v[8:9]
	v_lshl_add_u64 v[236:237], v[236:237], 0, v[2:3]
	v_lshl_add_u64 v[228:229], v[236:237], 0, s[24:25]
	v_lshl_add_u64 v[230:231], v[236:237], 0, s[12:13]
	v_lshl_add_u64 v[232:233], v[236:237], 0, s[26:27]
	v_lshl_add_u64 v[234:235], v[236:237], 0, s[28:29]
	v_lshl_add_u64 v[238:239], v[236:237], 0, s[30:31]
	v_lshl_add_u64 v[240:241], v[236:237], 0, s[34:35]
	v_lshl_add_u64 v[244:245], v[236:237], 0, s[36:37]
	global_load_dwordx4 v[196:199], v[236:237], off
	global_load_dwordx4 v[200:203], v[236:237], off offset:16
	global_load_dwordx4 v[204:207], v[236:237], off offset:512
	global_load_dwordx4 v[208:211], v[236:237], off offset:528
	global_load_dwordx4 v[212:215], v[228:229], off
	global_load_dwordx4 v[216:219], v[228:229], off offset:16
	global_load_dwordx4 v[220:223], v[228:229], off offset:512
	global_load_dwordx4 v[224:227], v[228:229], off offset:528
	s_waitcnt vmcnt(8)
	v_pk_mul_f32 v[10:11], v[6:7], s[22:23] op_sel_hi:[1,0]
	v_pk_mul_f32 v[12:13], v[4:5], s[22:23] op_sel_hi:[1,0]
	v_pk_mul_f32 v[20:21], v[20:21], s[22:23] op_sel_hi:[1,0]
	v_pk_mul_f32 v[4:5], v[26:27], s[22:23] op_sel_hi:[1,0]
	v_pk_mul_f32 v[6:7], v[24:25], s[22:23] op_sel_hi:[1,0]
	v_pk_mul_f32 v[14:15], v[30:31], s[22:23] op_sel_hi:[1,0]
	v_pk_mul_f32 v[16:17], v[28:29], s[22:23] op_sel_hi:[1,0]
	v_pk_mul_f32 v[18:19], v[22:23], s[22:23] op_sel_hi:[1,0]
	s_waitcnt vmcnt(7)
	v_pk_fma_f32 v[196:197], v[158:159], v[12:13], v[196:197]
	v_pk_fma_f32 v[198:199], v[160:161], v[10:11], v[198:199]
	v_lshl_add_u64 v[246:247], v[236:237], 0, s[48:49]
	global_store_dwordx4 v[246:247], v[196:199], off
	global_load_dwordx4 v[196:199], v[230:231], off
	s_waitcnt vmcnt(8)
	v_pk_fma_f32 v[200:201], v[154:155], v[6:7], v[200:201]
	v_pk_fma_f32 v[202:203], v[156:157], v[4:5], v[202:203]
	global_store_dwordx4 v[246:247], v[200:203], off offset:16
	global_load_dwordx4 v[200:203], v[230:231], off offset:16
	s_waitcnt vmcnt(9)
	v_pk_fma_f32 v[204:205], v[150:151], v[16:17], v[204:205]
	v_pk_fma_f32 v[206:207], v[152:153], v[14:15], v[206:207]
	global_store_dwordx4 v[246:247], v[204:207], off offset:512
	global_load_dwordx4 v[204:207], v[230:231], off offset:512
	s_waitcnt vmcnt(10)
	v_pk_fma_f32 v[208:209], v[138:139], v[20:21], v[208:209]
	v_pk_fma_f32 v[210:211], v[140:141], v[18:19], v[210:211]
	global_store_dwordx4 v[246:247], v[208:211], off offset:528
	global_load_dwordx4 v[208:211], v[230:231], off offset:528
	s_waitcnt vmcnt(11)
	v_pk_fma_f32 v[212:213], v[146:147], v[12:13], v[212:213]
	v_pk_fma_f32 v[214:215], v[148:149], v[10:11], v[214:215]
	v_lshl_add_u64 v[248:249], v[228:229], 0, s[48:49]
	global_store_dwordx4 v[248:249], v[212:215], off
	global_load_dwordx4 v[212:215], v[232:233], off
	s_waitcnt vmcnt(12)
	v_pk_fma_f32 v[216:217], v[142:143], v[6:7], v[216:217]
	v_pk_fma_f32 v[218:219], v[144:145], v[4:5], v[218:219]
	global_store_dwordx4 v[248:249], v[216:219], off offset:16
	global_load_dwordx4 v[216:219], v[232:233], off offset:16
	s_waitcnt vmcnt(13)
	v_pk_fma_f32 v[220:221], v[134:135], v[16:17], v[220:221]
	v_pk_fma_f32 v[222:223], v[136:137], v[14:15], v[222:223]
	global_store_dwordx4 v[248:249], v[220:223], off offset:512
	global_load_dwordx4 v[220:223], v[232:233], off offset:512
	s_waitcnt vmcnt(14)
	v_pk_fma_f32 v[224:225], v[122:123], v[20:21], v[224:225]
	v_pk_fma_f32 v[226:227], v[124:125], v[18:19], v[226:227]
	global_store_dwordx4 v[248:249], v[224:227], off offset:528
	global_load_dwordx4 v[224:227], v[232:233], off offset:528
	s_waitcnt vmcnt(14)
	v_pk_fma_f32 v[196:197], v[130:131], v[12:13], v[196:197]
	v_pk_fma_f32 v[198:199], v[132:133], v[10:11], v[198:199]
	v_lshl_add_u64 v[246:247], v[230:231], 0, s[48:49]
	global_store_dwordx4 v[246:247], v[196:199], off
	global_load_dwordx4 v[196:199], v[234:235], off
	s_waitcnt vmcnt(14)
	v_pk_fma_f32 v[200:201], v[126:127], v[6:7], v[200:201]
	v_pk_fma_f32 v[202:203], v[128:129], v[4:5], v[202:203]
	global_store_dwordx4 v[246:247], v[200:203], off offset:16
	global_load_dwordx4 v[200:203], v[234:235], off offset:16
	s_waitcnt vmcnt(14)
	v_pk_fma_f32 v[204:205], v[118:119], v[16:17], v[204:205]
	v_pk_fma_f32 v[206:207], v[120:121], v[14:15], v[206:207]
	global_store_dwordx4 v[246:247], v[204:207], off offset:512
	global_load_dwordx4 v[204:207], v[234:235], off offset:512
	s_waitcnt vmcnt(14)
	v_pk_fma_f32 v[208:209], v[106:107], v[20:21], v[208:209]
	v_pk_fma_f32 v[210:211], v[108:109], v[18:19], v[210:211]
	global_store_dwordx4 v[246:247], v[208:211], off offset:528
	global_load_dwordx4 v[208:211], v[234:235], off offset:528
	s_waitcnt vmcnt(14)
	v_pk_fma_f32 v[212:213], v[114:115], v[12:13], v[212:213]
	v_pk_fma_f32 v[214:215], v[116:117], v[10:11], v[214:215]
	v_lshl_add_u64 v[248:249], v[232:233], 0, s[48:49]
	global_store_dwordx4 v[248:249], v[212:215], off
	global_load_dwordx4 v[212:215], v[238:239], off
	s_waitcnt vmcnt(14)
	v_pk_fma_f32 v[216:217], v[110:111], v[6:7], v[216:217]
	v_pk_fma_f32 v[218:219], v[112:113], v[4:5], v[218:219]
	global_store_dwordx4 v[248:249], v[216:219], off offset:16
	global_load_dwordx4 v[216:219], v[238:239], off offset:16
	s_waitcnt vmcnt(14)
	v_pk_fma_f32 v[220:221], v[98:99], v[16:17], v[220:221]
	v_pk_fma_f32 v[222:223], v[100:101], v[14:15], v[222:223]
	global_store_dwordx4 v[248:249], v[220:223], off offset:512
	global_load_dwordx4 v[220:223], v[238:239], off offset:512
	s_waitcnt vmcnt(14)
	v_pk_fma_f32 v[224:225], v[90:91], v[20:21], v[224:225]
	v_pk_fma_f32 v[226:227], v[92:93], v[18:19], v[226:227]
	global_store_dwordx4 v[248:249], v[224:227], off offset:528
	global_load_dwordx4 v[224:227], v[238:239], off offset:528
	s_waitcnt vmcnt(14)
	v_pk_fma_f32 v[196:197], v[86:87], v[12:13], v[196:197]
	v_pk_fma_f32 v[198:199], v[88:89], v[10:11], v[198:199]
	v_lshl_add_u64 v[246:247], v[234:235], 0, s[48:49]
	global_store_dwordx4 v[246:247], v[196:199], off
	global_load_dwordx4 v[196:199], v[240:241], off
	s_waitcnt vmcnt(14)
	v_pk_fma_f32 v[200:201], v[78:79], v[6:7], v[200:201]
	v_pk_fma_f32 v[202:203], v[80:81], v[4:5], v[202:203]
	global_store_dwordx4 v[246:247], v[200:203], off offset:16
	global_load_dwordx4 v[200:203], v[240:241], off offset:16
	s_waitcnt vmcnt(14)
	v_pk_fma_f32 v[204:205], v[102:103], v[16:17], v[204:205]
	v_pk_fma_f32 v[206:207], v[104:105], v[14:15], v[206:207]
	global_store_dwordx4 v[246:247], v[204:207], off offset:512
	global_load_dwordx4 v[204:207], v[240:241], off offset:512
	s_waitcnt vmcnt(14)
	v_pk_fma_f32 v[208:209], v[94:95], v[20:21], v[208:209]
	v_pk_fma_f32 v[210:211], v[96:97], v[18:19], v[210:211]
	global_store_dwordx4 v[246:247], v[208:211], off offset:528
	global_load_dwordx4 v[208:211], v[240:241], off offset:528
	s_waitcnt vmcnt(14)
	v_pk_fma_f32 v[212:213], v[66:67], v[12:13], v[212:213]
	v_pk_fma_f32 v[214:215], v[68:69], v[10:11], v[214:215]
	v_lshl_add_u64 v[248:249], v[238:239], 0, s[48:49]
	global_store_dwordx4 v[248:249], v[212:215], off
	global_load_dwordx4 v[212:215], v[244:245], off
	s_waitcnt vmcnt(14)
	v_pk_fma_f32 v[216:217], v[58:59], v[6:7], v[216:217]
	v_pk_fma_f32 v[218:219], v[60:61], v[4:5], v[218:219]
	global_store_dwordx4 v[248:249], v[216:219], off offset:16
	global_load_dwordx4 v[216:219], v[244:245], off offset:16
	s_waitcnt vmcnt(14)
	v_pk_fma_f32 v[220:221], v[82:83], v[16:17], v[220:221]
	v_pk_fma_f32 v[222:223], v[84:85], v[14:15], v[222:223]
	global_store_dwordx4 v[248:249], v[220:223], off offset:512
	global_load_dwordx4 v[220:223], v[244:245], off offset:512
	s_waitcnt vmcnt(14)
	v_pk_fma_f32 v[224:225], v[74:75], v[20:21], v[224:225]
	v_pk_fma_f32 v[226:227], v[76:77], v[18:19], v[226:227]
	global_store_dwordx4 v[248:249], v[224:227], off offset:528
	global_load_dwordx4 v[224:227], v[244:245], off offset:528
	s_waitcnt vmcnt(14)
	v_pk_fma_f32 v[196:197], v[46:47], v[12:13], v[196:197]
	v_pk_fma_f32 v[198:199], v[48:49], v[10:11], v[198:199]
	v_lshl_add_u64 v[246:247], v[240:241], 0, s[48:49]
	global_store_dwordx4 v[246:247], v[196:199], off
	s_waitcnt vmcnt(13)
	v_pk_fma_f32 v[200:201], v[42:43], v[6:7], v[200:201]
	v_pk_fma_f32 v[202:203], v[44:45], v[4:5], v[202:203]
	global_store_dwordx4 v[246:247], v[200:203], off offset:16
	s_waitcnt vmcnt(12)
	v_pk_fma_f32 v[204:205], v[70:71], v[16:17], v[204:205]
	v_pk_fma_f32 v[206:207], v[72:73], v[14:15], v[206:207]
	global_store_dwordx4 v[246:247], v[204:207], off offset:512
	s_waitcnt vmcnt(11)
	v_pk_fma_f32 v[208:209], v[62:63], v[20:21], v[208:209]
	v_pk_fma_f32 v[210:211], v[64:65], v[18:19], v[210:211]
	global_store_dwordx4 v[246:247], v[208:211], off offset:528
	s_waitcnt vmcnt(10)
	v_pk_fma_f32 v[212:213], v[38:39], v[12:13], v[212:213]
	v_pk_fma_f32 v[214:215], v[40:41], v[10:11], v[214:215]
	v_lshl_add_u64 v[248:249], v[244:245], 0, s[48:49]
	global_store_dwordx4 v[248:249], v[212:215], off
	s_waitcnt vmcnt(9)
	v_pk_fma_f32 v[216:217], v[34:35], v[6:7], v[216:217]
	v_pk_fma_f32 v[218:219], v[36:37], v[4:5], v[218:219]
	global_store_dwordx4 v[248:249], v[216:219], off offset:16
	s_waitcnt vmcnt(8)
	v_pk_fma_f32 v[220:221], v[54:55], v[16:17], v[220:221]
	v_pk_fma_f32 v[222:223], v[56:57], v[14:15], v[222:223]
	global_store_dwordx4 v[248:249], v[220:223], off offset:512
	s_waitcnt vmcnt(7)
	v_pk_fma_f32 v[224:225], v[50:51], v[20:21], v[224:225]
	v_pk_fma_f32 v[226:227], v[52:53], v[18:19], v[226:227]
	global_store_dwordx4 v[248:249], v[224:227], off offset:528
	s_cbranch_vccnz .LBB0_747
	s_andn2_b64 vcc, exec, s[14:15]
	s_cbranch_vccnz .LBB0_746
	s_barrier
	s_branch .LBB0_746
